# attention tile loop: score masking in place, the 16+16 v_mov_b64 phi round-trip copies per tile removed
# baseline (speedup 1.0000x reference)
.LBB0_2682:
	s_andn2_b64 vcc, exec, s[12:13]
	s_cbranch_vccnz .LBB0_2690
	s_mov_b64 s[12:13], -1
	s_and_b64 vcc, exec, s[10:11]
	s_cbranch_vccz .LBB0_2685
	v_bfe_u32 v2, v217, s91, 1
	v_cmp_eq_u32_e32 vcc, 0, v2
	s_mov_b64 s[12:13], 0
	s_nop 0
	v_cndmask_b32_e32 v114, v114, v18, vcc
	v_cndmask_b32_e32 v98, v98, v18, vcc
	v_cndmask_b32_e32 v115, v115, v18, vcc
	v_cndmask_b32_e32 v99, v99, v18, vcc
	v_cndmask_b32_e32 v116, v116, v18, vcc
	v_cndmask_b32_e32 v100, v100, v18, vcc
	v_cndmask_b32_e32 v117, v117, v18, vcc
	v_cndmask_b32_e32 v101, v101, v18, vcc
	v_cndmask_b32_e32 v118, v118, v18, vcc
	v_cndmask_b32_e32 v102, v102, v18, vcc
	v_cndmask_b32_e32 v119, v119, v18, vcc
	v_cndmask_b32_e32 v103, v103, v18, vcc
	v_cndmask_b32_e32 v120, v120, v18, vcc
	v_cndmask_b32_e32 v104, v104, v18, vcc
	v_cndmask_b32_e32 v121, v121, v18, vcc
	v_cndmask_b32_e32 v105, v105, v18, vcc
	v_cndmask_b32_e32 v122, v122, v18, vcc
	v_cndmask_b32_e32 v106, v106, v18, vcc
	v_cndmask_b32_e32 v123, v123, v18, vcc
	v_cndmask_b32_e32 v107, v107, v18, vcc
	v_cndmask_b32_e32 v124, v124, v18, vcc
	v_cndmask_b32_e32 v108, v108, v18, vcc
	v_cndmask_b32_e32 v125, v125, v18, vcc
	v_cndmask_b32_e32 v109, v109, v18, vcc
	v_cndmask_b32_e32 v126, v126, v18, vcc
	v_cndmask_b32_e32 v110, v110, v18, vcc
	v_cndmask_b32_e32 v127, v127, v18, vcc
	v_cndmask_b32_e32 v111, v111, v18, vcc
	v_cndmask_b32_e32 v128, v128, v18, vcc
	v_cndmask_b32_e32 v112, v112, v18, vcc
	v_cndmask_b32_e32 v129, v129, v18, vcc
	v_cndmask_b32_e32 v113, v113, v18, vcc
.LBB0_2685:
	s_andn2_b64 vcc, exec, s[12:13]
	s_cbranch_vccnz .LBB0_2690
	s_or_b32 s3, s95, 63
	s_cmp_le_i32 s3, s81
	s_cbranch_scc1 .LBB0_2688
	v_subrev_u32_e32 v2, s95, v218
	v_cmp_gt_i32_e64 s[68:69], 26, v2
	v_cmp_gt_i32_e64 s[70:71], 27, v2
	v_cmp_gt_i32_e64 s[66:67], 25, v2
	s_and_b64 s[68:69], s[70:71], s[68:69]
	v_cmp_gt_i32_e64 s[64:65], 24, v2
	s_and_b64 s[66:67], s[68:69], s[66:67]
	v_cmp_gt_i32_e64 s[62:63], 19, v2
	s_and_b64 s[64:65], s[66:67], s[64:65]
	v_cmp_gt_i32_e64 s[60:61], 18, v2
	s_and_b64 s[62:63], s[64:65], s[62:63]
	v_cmp_gt_i32_e64 s[58:59], 17, v2
	s_and_b64 s[60:61], s[62:63], s[60:61]
	v_cmp_gt_i32_e64 s[56:57], 16, v2
	s_and_b64 s[58:59], s[60:61], s[58:59]
	v_cmp_gt_i32_e64 s[54:55], 11, v2
	s_and_b64 s[56:57], s[58:59], s[56:57]
	v_cmp_gt_i32_e64 s[52:53], 10, v2
	s_and_b64 s[54:55], s[56:57], s[54:55]
	v_cmp_gt_i32_e64 s[50:51], 9, v2
	s_and_b64 s[52:53], s[54:55], s[52:53]
	v_cmp_gt_i32_e64 s[48:49], 8, v2
	s_and_b64 s[50:51], s[52:53], s[50:51]
	v_cmp_gt_i32_e64 s[46:47], 3, v2
	s_and_b64 s[48:49], s[50:51], s[48:49]
	v_cmp_gt_i32_e64 s[44:45], 2, v2
	s_and_b64 s[46:47], s[48:49], s[46:47]
	v_cmp_gt_i32_e64 s[42:43], 1, v2
	s_and_b64 s[44:45], s[46:47], s[44:45]
	v_cmp_gt_i32_e64 s[40:41], 0, v2
	s_and_b64 s[42:43], s[44:45], s[42:43]
	s_and_b64 s[40:41], s[42:43], s[40:41]
	v_cmp_gt_i32_e64 s[38:39], 58, v2
	v_cndmask_b32_e64 v114, v114, v18, s[40:41]
	v_cmp_gt_i32_e64 s[40:41], 59, v2
	v_cmp_gt_i32_e64 s[36:37], 57, v2
	s_and_b64 s[38:39], s[40:41], s[38:39]
	v_cmp_gt_i32_e64 s[34:35], 56, v2
	s_and_b64 s[36:37], s[38:39], s[36:37]
	v_cmp_gt_i32_e64 s[30:31], 51, v2
	s_and_b64 s[34:35], s[36:37], s[34:35]
	v_cmp_gt_i32_e64 s[28:29], 50, v2
	s_and_b64 s[30:31], s[34:35], s[30:31]
	v_cmp_gt_i32_e64 s[26:27], 49, v2
	s_and_b64 s[28:29], s[30:31], s[28:29]
	v_cmp_gt_i32_e64 s[24:25], 48, v2
	s_and_b64 s[26:27], s[28:29], s[26:27]
	v_cmp_gt_i32_e64 s[22:23], 43, v2
	s_and_b64 s[24:25], s[26:27], s[24:25]
	v_cmp_gt_i32_e64 s[20:21], 42, v2
	s_and_b64 s[22:23], s[24:25], s[22:23]
	v_cmp_gt_i32_e64 s[18:19], 41, v2
	s_and_b64 s[20:21], s[22:23], s[20:21]
	v_cmp_gt_i32_e64 s[16:17], 40, v2
	s_and_b64 s[18:19], s[20:21], s[18:19]
	v_cmp_gt_i32_e64 s[14:15], 35, v2
	s_and_b64 s[16:17], s[18:19], s[16:17]
	v_cmp_gt_i32_e64 s[12:13], 34, v2
	s_and_b64 s[14:15], s[16:17], s[14:15]
	v_cmp_gt_i32_e64 s[10:11], 33, v2
	s_and_b64 s[12:13], s[14:15], s[12:13]
	v_cmp_gt_i32_e32 vcc, 32, v2
	s_and_b64 s[10:11], s[12:13], s[10:11]
	v_cndmask_b32_e64 v127, v127, v18, s[66:67]
	v_cndmask_b32_e64 v126, v126, v18, s[64:65]
	v_cndmask_b32_e64 v125, v125, v18, s[62:63]
	v_cndmask_b32_e64 v124, v124, v18, s[60:61]
	v_readlane_b32 s60, v254, 55
	v_cndmask_b32_e64 v123, v123, v18, s[58:59]
	v_cndmask_b32_e64 v122, v122, v18, s[56:57]
	v_readlane_b32 s56, v254, 51
	s_and_b64 vcc, s[10:11], vcc
	v_cndmask_b32_e64 v129, v129, v18, s[70:71]
	v_cndmask_b32_e64 v128, v128, v18, s[68:69]
	v_readlane_b32 s61, v254, 56
	v_readlane_b32 s64, v254, 59
	v_readlane_b32 s65, v254, 60
	v_readlane_b32 s66, v254, 61
	v_readlane_b32 s67, v254, 62
	v_readlane_b32 s57, v254, 52
	v_cndmask_b32_e64 v121, v121, v18, s[54:55]
	v_cndmask_b32_e64 v120, v120, v18, s[52:53]
	v_cndmask_b32_e64 v119, v119, v18, s[50:51]
	v_cndmask_b32_e64 v118, v118, v18, s[48:49]
	v_cndmask_b32_e64 v117, v117, v18, s[46:47]
	v_cndmask_b32_e64 v116, v116, v18, s[44:45]
	v_cndmask_b32_e64 v115, v115, v18, s[42:43]
	v_cndmask_b32_e64 v113, v113, v18, s[40:41]
	v_cndmask_b32_e64 v112, v112, v18, s[38:39]
	v_cndmask_b32_e64 v111, v111, v18, s[36:37]
	v_cndmask_b32_e64 v110, v110, v18, s[34:35]
	v_cndmask_b32_e64 v109, v109, v18, s[30:31]
	v_cndmask_b32_e64 v108, v108, v18, s[28:29]
	v_cndmask_b32_e64 v107, v107, v18, s[26:27]
	v_cndmask_b32_e64 v106, v106, v18, s[24:25]
	v_cndmask_b32_e64 v105, v105, v18, s[22:23]
	v_cndmask_b32_e64 v104, v104, v18, s[20:21]
	v_cndmask_b32_e64 v103, v103, v18, s[18:19]
	v_cndmask_b32_e64 v102, v102, v18, s[16:17]
	v_cndmask_b32_e64 v101, v101, v18, s[14:15]
	v_cndmask_b32_e64 v100, v100, v18, s[12:13]
	v_cndmask_b32_e64 v99, v99, v18, s[10:11]
	v_cndmask_b32_e32 v98, v98, v18, vcc
	v_readlane_b32 s62, v254, 57
	v_readlane_b32 s63, v254, 58
	v_readlane_b32 s58, v254, 53
	v_readlane_b32 s59, v254, 54
.LBB0_2688:
	s_branch .LBB0_2690
.LBB0_2690:
	v_max_f32_e32 v2, v115, v115
	v_max_f32_e32 v19, v114, v114
	v_max_f32_e32 v2, v19, v2
	v_max3_f32 v2, v2, v116, v117
	v_max3_f32 v2, v2, v118, v119
	v_max3_f32 v2, v2, v120, v121
	v_max3_f32 v2, v2, v122, v123
	v_max3_f32 v2, v2, v124, v125
	v_max3_f32 v2, v2, v126, v127
	v_max3_f32 v2, v2, v128, v129
	v_max3_f32 v2, v2, v98, v99
	v_max3_f32 v2, v2, v100, v101
	v_max3_f32 v2, v2, v102, v103
	v_max3_f32 v2, v2, v104, v105
	v_max3_f32 v2, v2, v106, v107
	v_max3_f32 v2, v2, v108, v109
	v_max3_f32 v2, v2, v110, v111
	v_max3_f32 v2, v2, v112, v113
	v_mov_b32_e32 v19, v2
	s_nop 1
	v_permlane32_swap_b32_e32 v2, v19
	v_max_f32_e32 v19, v19, v19
	v_max_f32_e32 v2, v2, v2
	v_max_f32_e32 v2, v2, v19
	v_sub_f32_e32 v19, v2, v219
	v_mul_f32_e32 v19, 0x3db504f3, v19
	v_cmp_ge_f32_e32 vcc, s1, v19
	v_max_f32_e32 v19, v219, v219
	v_max_f32_e32 v2, v19, v2
	v_sub_f32_e32 v19, v219, v2
	v_mul_f32_e32 v19, 0x3e0293ee, v19
	v_exp_f32_e32 v19, v19
	s_cmp_eq_u64 vcc, exec
	s_cselect_b64 s[10:11], -1, 0
	s_barrier
	s_waitcnt vmcnt(0)
	v_cndmask_b32_e64 v220, v19, 1.0, s[10:11]
	v_cmp_gt_f32_e32 vcc, 1.0, v220
	s_waitcnt vmcnt(3)
	ds_write_b128 v205, v[4:7]
	s_waitcnt vmcnt(2)
	ds_write_b128 v206, v[8:11]
	s_waitcnt vmcnt(1)
	ds_write_b128 v211, v[12:15] offset:32768
	s_waitcnt vmcnt(0)
	ds_write_b128 v211, v[178:181] offset:40960
	s_cbranch_vccz .LBB0_2694
	s_and_saveexec_b64 s[12:13], s[4:5]
	ds_write_b32 v215, v220 offset:128
	s_or_b64 exec, exec, s[12:13]
	s_waitcnt lgkmcnt(0)
	ds_read_b128 v[20:23], v214 offset:224
	ds_read_b128 v[24:27], v214 offset:192
	ds_read_b128 v[28:31], v214 offset:160
	ds_read_b128 v[130:133], v214 offset:128
	s_waitcnt lgkmcnt(3)
	v_pk_mul_f32 v[96:97], v[96:97], v[22:23]
	s_waitcnt lgkmcnt(2)
	v_pk_mul_f32 v[92:93], v[92:93], v[26:27]
	s_waitcnt lgkmcnt(1)
	v_pk_mul_f32 v[88:89], v[88:89], v[30:31]
	s_waitcnt lgkmcnt(0)
	v_pk_mul_f32 v[84:85], v[84:85], v[132:133]
	v_pk_mul_f32 v[94:95], v[94:95], v[20:21]
	v_pk_mul_f32 v[90:91], v[90:91], v[24:25]
	v_pk_mul_f32 v[86:87], v[86:87], v[28:29]
	v_pk_mul_f32 v[82:83], v[82:83], v[130:131]
	v_pk_mul_f32 v[80:81], v[80:81], v[22:23]
	v_pk_mul_f32 v[76:77], v[76:77], v[26:27]
	v_pk_mul_f32 v[72:73], v[72:73], v[30:31]
	v_pk_mul_f32 v[68:69], v[68:69], v[132:133]
	v_pk_mul_f32 v[78:79], v[78:79], v[20:21]
	v_pk_mul_f32 v[74:75], v[74:75], v[24:25]
	v_pk_mul_f32 v[70:71], v[70:71], v[28:29]
	v_pk_mul_f32 v[66:67], v[66:67], v[130:131]
	v_pk_mul_f32 v[64:65], v[64:65], v[22:23]
	v_pk_mul_f32 v[60:61], v[60:61], v[26:27]
	v_pk_mul_f32 v[56:57], v[56:57], v[30:31]
	v_pk_mul_f32 v[52:53], v[52:53], v[132:133]
	v_pk_mul_f32 v[62:63], v[62:63], v[20:21]
	v_pk_mul_f32 v[58:59], v[58:59], v[24:25]
	v_pk_mul_f32 v[54:55], v[54:55], v[28:29]
	v_pk_mul_f32 v[50:51], v[50:51], v[130:131]
	v_pk_mul_f32 v[48:49], v[48:49], v[22:23]
	v_pk_mul_f32 v[44:45], v[44:45], v[26:27]
	v_pk_mul_f32 v[40:41], v[40:41], v[30:31]
	v_pk_mul_f32 v[36:37], v[36:37], v[132:133]
	v_pk_mul_f32 v[46:47], v[46:47], v[20:21]
	v_pk_mul_f32 v[42:43], v[42:43], v[24:25]
	v_pk_mul_f32 v[38:39], v[38:39], v[28:29]
	v_pk_mul_f32 v[34:35], v[34:35], v[130:131]

.LBB0_2709:
	s_andn2_b64 vcc, exec, s[8:9]
	s_cbranch_vccnz .LBB0_2717
	s_mov_b64 s[8:9], -1
	s_and_b64 vcc, exec, s[10:11]
	s_cbranch_vccz .LBB0_2712
	v_bfe_u32 v2, v217, s2, 1
	v_cmp_eq_u32_e32 vcc, 0, v2
	s_mov_b64 s[8:9], 0
	s_nop 0
	v_cndmask_b32_e32 v114, v114, v18, vcc
	v_cndmask_b32_e32 v98, v98, v18, vcc
	v_cndmask_b32_e32 v115, v115, v18, vcc
	v_cndmask_b32_e32 v99, v99, v18, vcc
	v_cndmask_b32_e32 v116, v116, v18, vcc
	v_cndmask_b32_e32 v100, v100, v18, vcc
	v_cndmask_b32_e32 v117, v117, v18, vcc
	v_cndmask_b32_e32 v101, v101, v18, vcc
	v_cndmask_b32_e32 v118, v118, v18, vcc
	v_cndmask_b32_e32 v102, v102, v18, vcc
	v_cndmask_b32_e32 v119, v119, v18, vcc
	v_cndmask_b32_e32 v103, v103, v18, vcc
	v_cndmask_b32_e32 v120, v120, v18, vcc
	v_cndmask_b32_e32 v104, v104, v18, vcc
	v_cndmask_b32_e32 v121, v121, v18, vcc
	v_cndmask_b32_e32 v105, v105, v18, vcc
	v_cndmask_b32_e32 v122, v122, v18, vcc
	v_cndmask_b32_e32 v106, v106, v18, vcc
	v_cndmask_b32_e32 v123, v123, v18, vcc
	v_cndmask_b32_e32 v107, v107, v18, vcc
	v_cndmask_b32_e32 v124, v124, v18, vcc
	v_cndmask_b32_e32 v108, v108, v18, vcc
	v_cndmask_b32_e32 v125, v125, v18, vcc
	v_cndmask_b32_e32 v109, v109, v18, vcc
	v_cndmask_b32_e32 v126, v126, v18, vcc
	v_cndmask_b32_e32 v110, v110, v18, vcc
	v_cndmask_b32_e32 v127, v127, v18, vcc
	v_cndmask_b32_e32 v111, v111, v18, vcc
	v_cndmask_b32_e32 v128, v128, v18, vcc
	v_cndmask_b32_e32 v112, v112, v18, vcc
	v_cndmask_b32_e32 v129, v129, v18, vcc
	v_cndmask_b32_e32 v113, v113, v18, vcc
.LBB0_2712:
	s_andn2_b64 vcc, exec, s[8:9]
	s_cbranch_vccnz .LBB0_2717
	s_or_b32 s2, s3, 63
	s_cmp_le_i32 s2, s81
	s_cbranch_scc1 .LBB0_2715
	v_subrev_u32_e32 v2, s3, v218
	v_cmp_gt_i32_e64 s[66:67], 26, v2
	v_cmp_gt_i32_e64 s[68:69], 27, v2
	v_cmp_gt_i32_e64 s[64:65], 25, v2
	s_and_b64 s[66:67], s[68:69], s[66:67]
	v_cmp_gt_i32_e64 s[62:63], 24, v2
	s_and_b64 s[64:65], s[66:67], s[64:65]
	v_cmp_gt_i32_e64 s[60:61], 19, v2
	s_and_b64 s[62:63], s[64:65], s[62:63]
	v_cmp_gt_i32_e64 s[58:59], 18, v2
	s_and_b64 s[60:61], s[62:63], s[60:61]
	v_cmp_gt_i32_e64 s[56:57], 17, v2
	s_and_b64 s[58:59], s[60:61], s[58:59]
	v_cmp_gt_i32_e64 s[54:55], 16, v2
	s_and_b64 s[56:57], s[58:59], s[56:57]
	v_cmp_gt_i32_e64 s[52:53], 11, v2
	s_and_b64 s[54:55], s[56:57], s[54:55]
	v_cmp_gt_i32_e64 s[50:51], 10, v2
	s_and_b64 s[52:53], s[54:55], s[52:53]
	v_cmp_gt_i32_e64 s[48:49], 9, v2
	s_and_b64 s[50:51], s[52:53], s[50:51]
	v_cmp_gt_i32_e64 s[46:47], 8, v2
	s_and_b64 s[48:49], s[50:51], s[48:49]
	v_cmp_gt_i32_e64 s[44:45], 3, v2
	s_and_b64 s[46:47], s[48:49], s[46:47]
	v_cmp_gt_i32_e64 s[42:43], 2, v2
	s_and_b64 s[44:45], s[46:47], s[44:45]
	v_cmp_gt_i32_e64 s[40:41], 1, v2
	s_and_b64 s[42:43], s[44:45], s[42:43]
	v_cmp_gt_i32_e64 s[38:39], 0, v2
	s_and_b64 s[40:41], s[42:43], s[40:41]
	s_and_b64 s[38:39], s[40:41], s[38:39]
	v_cmp_gt_i32_e64 s[36:37], 58, v2
	v_cndmask_b32_e64 v114, v114, v18, s[38:39]
	v_cmp_gt_i32_e64 s[38:39], 59, v2
	v_cmp_gt_i32_e64 s[34:35], 57, v2
	s_and_b64 s[36:37], s[38:39], s[36:37]
	v_cmp_gt_i32_e64 s[30:31], 56, v2
	s_and_b64 s[34:35], s[36:37], s[34:35]
	v_cmp_gt_i32_e64 s[28:29], 51, v2
	s_and_b64 s[30:31], s[34:35], s[30:31]
	v_cmp_gt_i32_e64 s[26:27], 50, v2
	s_and_b64 s[28:29], s[30:31], s[28:29]
	v_cmp_gt_i32_e64 s[24:25], 49, v2
	s_and_b64 s[26:27], s[28:29], s[26:27]
	v_cmp_gt_i32_e64 s[22:23], 48, v2
	s_and_b64 s[24:25], s[26:27], s[24:25]
	v_cmp_gt_i32_e64 s[20:21], 43, v2
	s_and_b64 s[22:23], s[24:25], s[22:23]
	v_cmp_gt_i32_e64 s[18:19], 42, v2
	s_and_b64 s[20:21], s[22:23], s[20:21]
	v_cmp_gt_i32_e64 s[16:17], 41, v2
	s_and_b64 s[18:19], s[20:21], s[18:19]
	v_cmp_gt_i32_e64 s[14:15], 40, v2
	s_and_b64 s[16:17], s[18:19], s[16:17]
	v_cmp_gt_i32_e64 s[12:13], 35, v2
	s_and_b64 s[14:15], s[16:17], s[14:15]
	v_cmp_gt_i32_e64 s[10:11], 34, v2
	s_and_b64 s[12:13], s[14:15], s[12:13]
	v_cmp_gt_i32_e64 s[8:9], 33, v2
	s_and_b64 s[10:11], s[12:13], s[10:11]
	v_cmp_gt_i32_e32 vcc, 32, v2
	s_and_b64 s[8:9], s[10:11], s[8:9]
	v_cndmask_b32_e64 v128, v128, v18, s[66:67]
	v_cndmask_b32_e64 v127, v127, v18, s[64:65]
	v_cndmask_b32_e64 v126, v126, v18, s[62:63]
	v_cndmask_b32_e64 v125, v125, v18, s[60:61]
	v_readlane_b32 s60, v254, 55
	v_cndmask_b32_e64 v124, v124, v18, s[58:59]
	v_cndmask_b32_e64 v123, v123, v18, s[56:57]
	v_readlane_b32 s56, v254, 51
	s_and_b64 vcc, s[8:9], vcc
	v_cndmask_b32_e64 v129, v129, v18, s[68:69]
	v_readlane_b32 s61, v254, 56
	v_readlane_b32 s64, v254, 59
	v_readlane_b32 s65, v254, 60
	v_readlane_b32 s66, v254, 61
	v_readlane_b32 s67, v254, 62
	v_readlane_b32 s57, v254, 52
	v_cndmask_b32_e64 v122, v122, v18, s[54:55]
	v_cndmask_b32_e64 v121, v121, v18, s[52:53]
	v_cndmask_b32_e64 v120, v120, v18, s[50:51]
	v_cndmask_b32_e64 v119, v119, v18, s[48:49]
	v_cndmask_b32_e64 v118, v118, v18, s[46:47]
	v_cndmask_b32_e64 v117, v117, v18, s[44:45]
	v_cndmask_b32_e64 v116, v116, v18, s[42:43]
	v_cndmask_b32_e64 v115, v115, v18, s[40:41]
	v_cndmask_b32_e64 v113, v113, v18, s[38:39]
	v_cndmask_b32_e64 v112, v112, v18, s[36:37]
	v_cndmask_b32_e64 v111, v111, v18, s[34:35]
	v_cndmask_b32_e64 v110, v110, v18, s[30:31]
	v_cndmask_b32_e64 v109, v109, v18, s[28:29]
	v_cndmask_b32_e64 v108, v108, v18, s[26:27]
	v_cndmask_b32_e64 v107, v107, v18, s[24:25]
	v_cndmask_b32_e64 v106, v106, v18, s[22:23]
	v_cndmask_b32_e64 v105, v105, v18, s[20:21]
	v_cndmask_b32_e64 v104, v104, v18, s[18:19]
	v_cndmask_b32_e64 v103, v103, v18, s[16:17]
	v_cndmask_b32_e64 v102, v102, v18, s[14:15]
	v_cndmask_b32_e64 v101, v101, v18, s[12:13]
	v_cndmask_b32_e64 v100, v100, v18, s[10:11]
	v_cndmask_b32_e64 v99, v99, v18, s[8:9]
	v_cndmask_b32_e32 v98, v98, v18, vcc
	v_readlane_b32 s62, v254, 57
	v_readlane_b32 s63, v254, 58
	v_readlane_b32 s58, v254, 53
	v_readlane_b32 s59, v254, 54
.LBB0_2715:
	s_branch .LBB0_2717
.LBB0_2717:
	v_max_f32_e32 v2, v115, v115
	v_max_f32_e32 v20, v114, v114
	v_max_f32_e32 v2, v20, v2
	v_max3_f32 v2, v2, v116, v117
	v_max3_f32 v2, v2, v118, v119
	v_max3_f32 v2, v2, v120, v121
	v_max3_f32 v2, v2, v122, v123
	v_max3_f32 v2, v2, v124, v125
	v_max3_f32 v2, v2, v126, v127
	v_max3_f32 v2, v2, v128, v129
	v_max3_f32 v2, v2, v98, v99
	v_max3_f32 v2, v2, v100, v101
	v_max3_f32 v2, v2, v102, v103
	v_max3_f32 v2, v2, v104, v105
	v_max3_f32 v2, v2, v106, v107
	v_max3_f32 v2, v2, v108, v109
	v_max3_f32 v2, v2, v110, v111
	v_max3_f32 v2, v2, v112, v113
	v_mov_b32_e32 v20, v2
	s_nop 1
	v_permlane32_swap_b32_e32 v2, v20
	v_max_f32_e32 v20, v20, v20
	v_max_f32_e32 v2, v2, v2
	v_max_f32_e32 v2, v2, v20
	v_sub_f32_e32 v20, v2, v219
	v_mul_f32_e32 v20, 0x3db504f3, v20
	v_cmp_ge_f32_e32 vcc, s1, v20
	s_cmp_eq_u64 vcc, exec
	s_cselect_b64 s[8:9], -1, 0
	s_andn2_b64 vcc, exec, s[70:71]
	s_barrier
	s_cbranch_vccnz .LBB0_2719
	s_waitcnt vmcnt(0)
	s_waitcnt vmcnt(3)
	ds_write_b128 v205, v[4:7] offset:16384
	s_waitcnt vmcnt(2)
	ds_write_b128 v206, v[8:11] offset:16384
	s_waitcnt vmcnt(1)
	ds_write_b128 v211, v[12:15] offset:49152
	s_waitcnt vmcnt(0)
	ds_write_b128 v211, v[178:181] offset:57344

.LBB0_3249:
	s_andn2_b64 vcc, exec, s[12:13]
	s_cbranch_vccnz .LBB0_3257
	s_mov_b64 s[12:13], -1
	s_and_b64 vcc, exec, s[10:11]
	s_cbranch_vccz .LBB0_3252
	v_bfe_u32 v2, v213, s3, 1
	v_cmp_eq_u32_e32 vcc, 0, v2
	s_mov_b64 s[12:13], 0
	s_nop 0
	v_cndmask_b32_e32 v114, v114, v18, vcc
	v_cndmask_b32_e32 v98, v98, v18, vcc
	v_cndmask_b32_e32 v115, v115, v18, vcc
	v_cndmask_b32_e32 v99, v99, v18, vcc
	v_cndmask_b32_e32 v116, v116, v18, vcc
	v_cndmask_b32_e32 v100, v100, v18, vcc
	v_cndmask_b32_e32 v117, v117, v18, vcc
	v_cndmask_b32_e32 v101, v101, v18, vcc
	v_cndmask_b32_e32 v118, v118, v18, vcc
	v_cndmask_b32_e32 v102, v102, v18, vcc
	v_cndmask_b32_e32 v119, v119, v18, vcc
	v_cndmask_b32_e32 v103, v103, v18, vcc
	v_cndmask_b32_e32 v120, v120, v18, vcc
	v_cndmask_b32_e32 v104, v104, v18, vcc
	v_cndmask_b32_e32 v121, v121, v18, vcc
	v_cndmask_b32_e32 v105, v105, v18, vcc
	v_cndmask_b32_e32 v122, v122, v18, vcc
	v_cndmask_b32_e32 v106, v106, v18, vcc
	v_cndmask_b32_e32 v123, v123, v18, vcc
	v_cndmask_b32_e32 v107, v107, v18, vcc
	v_cndmask_b32_e32 v124, v124, v18, vcc
	v_cndmask_b32_e32 v108, v108, v18, vcc
	v_cndmask_b32_e32 v125, v125, v18, vcc
	v_cndmask_b32_e32 v109, v109, v18, vcc
	v_cndmask_b32_e32 v126, v126, v18, vcc
	v_cndmask_b32_e32 v110, v110, v18, vcc
	v_cndmask_b32_e32 v127, v127, v18, vcc
	v_cndmask_b32_e32 v111, v111, v18, vcc
	v_cndmask_b32_e32 v128, v128, v18, vcc
	v_cndmask_b32_e32 v112, v112, v18, vcc
	v_cndmask_b32_e32 v129, v129, v18, vcc
	v_cndmask_b32_e32 v113, v113, v18, vcc
.LBB0_3252:
	s_andn2_b64 vcc, exec, s[12:13]
	s_cbranch_vccnz .LBB0_3257
	s_or_b32 s10, s95, 63
	s_cmp_le_i32 s10, s82
	s_cbranch_scc1 .LBB0_3255
	v_subrev_u32_e32 v2, s95, v214
	v_cmp_gt_i32_e64 s[68:69], 26, v2
	v_cmp_gt_i32_e64 s[70:71], 27, v2
	v_cmp_gt_i32_e64 s[66:67], 25, v2
	s_and_b64 s[68:69], s[70:71], s[68:69]
	v_cmp_gt_i32_e64 s[64:65], 24, v2
	s_and_b64 s[66:67], s[68:69], s[66:67]
	v_cmp_gt_i32_e64 s[62:63], 19, v2
	s_and_b64 s[64:65], s[66:67], s[64:65]
	v_cmp_gt_i32_e64 s[60:61], 18, v2
	s_and_b64 s[62:63], s[64:65], s[62:63]
	v_cmp_gt_i32_e64 s[58:59], 17, v2
	s_and_b64 s[60:61], s[62:63], s[60:61]
	v_cmp_gt_i32_e64 s[56:57], 16, v2
	s_and_b64 s[58:59], s[60:61], s[58:59]
	v_cmp_gt_i32_e64 s[54:55], 11, v2
	s_and_b64 s[56:57], s[58:59], s[56:57]
	v_cmp_gt_i32_e64 s[52:53], 10, v2
	s_and_b64 s[54:55], s[56:57], s[54:55]
	v_cmp_gt_i32_e64 s[50:51], 9, v2
	s_and_b64 s[52:53], s[54:55], s[52:53]
	v_cmp_gt_i32_e64 s[48:49], 8, v2
	s_and_b64 s[50:51], s[52:53], s[50:51]
	v_cmp_gt_i32_e64 s[46:47], 3, v2
	s_and_b64 s[48:49], s[50:51], s[48:49]
	v_cmp_gt_i32_e64 s[44:45], 2, v2
	s_and_b64 s[46:47], s[48:49], s[46:47]
	v_cmp_gt_i32_e64 s[42:43], 1, v2
	s_and_b64 s[44:45], s[46:47], s[44:45]
	v_cmp_gt_i32_e64 s[40:41], 0, v2
	s_and_b64 s[42:43], s[44:45], s[42:43]
	s_and_b64 s[40:41], s[42:43], s[40:41]
	v_cmp_gt_i32_e64 s[38:39], 58, v2
	v_cndmask_b32_e64 v114, v114, v18, s[40:41]
	v_cmp_gt_i32_e64 s[40:41], 59, v2
	v_cmp_gt_i32_e64 s[36:37], 57, v2
	s_and_b64 s[38:39], s[40:41], s[38:39]
	v_cmp_gt_i32_e64 s[34:35], 56, v2
	s_and_b64 s[36:37], s[38:39], s[36:37]
	v_cmp_gt_i32_e64 s[30:31], 51, v2
	s_and_b64 s[34:35], s[36:37], s[34:35]
	v_cmp_gt_i32_e64 s[28:29], 50, v2
	s_and_b64 s[30:31], s[34:35], s[30:31]
	v_cmp_gt_i32_e64 s[26:27], 49, v2
	s_and_b64 s[28:29], s[30:31], s[28:29]
	v_cmp_gt_i32_e64 s[24:25], 48, v2
	s_and_b64 s[26:27], s[28:29], s[26:27]
	v_cmp_gt_i32_e64 s[22:23], 43, v2
	s_and_b64 s[24:25], s[26:27], s[24:25]
	v_cmp_gt_i32_e64 s[20:21], 42, v2
	s_and_b64 s[22:23], s[24:25], s[22:23]
	v_cmp_gt_i32_e64 s[18:19], 41, v2
	s_and_b64 s[20:21], s[22:23], s[20:21]
	v_cmp_gt_i32_e64 s[16:17], 40, v2
	s_and_b64 s[18:19], s[20:21], s[18:19]
	v_cmp_gt_i32_e64 s[14:15], 35, v2
	s_and_b64 s[16:17], s[18:19], s[16:17]
	v_cmp_gt_i32_e64 s[12:13], 34, v2
	s_and_b64 s[14:15], s[16:17], s[14:15]
	v_cmp_gt_i32_e64 s[10:11], 33, v2
	s_and_b64 s[12:13], s[14:15], s[12:13]
	v_cmp_gt_i32_e32 vcc, 32, v2
	s_and_b64 s[10:11], s[12:13], s[10:11]
	v_cndmask_b32_e64 v127, v127, v18, s[66:67]
	v_cndmask_b32_e64 v126, v126, v18, s[64:65]
	v_cndmask_b32_e64 v125, v125, v18, s[62:63]
	v_cndmask_b32_e64 v124, v124, v18, s[60:61]
	v_readlane_b32 s60, v254, 55
	v_cndmask_b32_e64 v123, v123, v18, s[58:59]
	v_cndmask_b32_e64 v122, v122, v18, s[56:57]
	v_readlane_b32 s56, v254, 51
	s_and_b64 vcc, s[10:11], vcc
	v_cndmask_b32_e64 v129, v129, v18, s[70:71]
	v_cndmask_b32_e64 v128, v128, v18, s[68:69]
	v_readlane_b32 s61, v254, 56
	v_readlane_b32 s57, v254, 52
	v_cndmask_b32_e64 v121, v121, v18, s[54:55]
	v_cndmask_b32_e64 v120, v120, v18, s[52:53]
	v_cndmask_b32_e64 v119, v119, v18, s[50:51]
	v_cndmask_b32_e64 v118, v118, v18, s[48:49]
	v_cndmask_b32_e64 v117, v117, v18, s[46:47]
	v_cndmask_b32_e64 v116, v116, v18, s[44:45]
	v_cndmask_b32_e64 v115, v115, v18, s[42:43]
	v_cndmask_b32_e64 v113, v113, v18, s[40:41]
	v_cndmask_b32_e64 v112, v112, v18, s[38:39]
	v_cndmask_b32_e64 v111, v111, v18, s[36:37]
	v_cndmask_b32_e64 v110, v110, v18, s[34:35]
	v_cndmask_b32_e64 v109, v109, v18, s[30:31]
	v_cndmask_b32_e64 v108, v108, v18, s[28:29]
	v_cndmask_b32_e64 v107, v107, v18, s[26:27]
	v_cndmask_b32_e64 v106, v106, v18, s[24:25]
	v_cndmask_b32_e64 v105, v105, v18, s[22:23]
	v_cndmask_b32_e64 v104, v104, v18, s[20:21]
	v_cndmask_b32_e64 v103, v103, v18, s[18:19]
	v_cndmask_b32_e64 v102, v102, v18, s[16:17]
	v_cndmask_b32_e64 v101, v101, v18, s[14:15]
	v_cndmask_b32_e64 v100, v100, v18, s[12:13]
	v_cndmask_b32_e64 v99, v99, v18, s[10:11]
	v_cndmask_b32_e32 v98, v98, v18, vcc
	v_readlane_b32 s62, v254, 57
	v_readlane_b32 s63, v254, 58
	v_readlane_b32 s64, v254, 59
	v_readlane_b32 s65, v254, 60
	v_readlane_b32 s66, v254, 61
	v_readlane_b32 s67, v254, 62
	v_readlane_b32 s58, v254, 53
	v_readlane_b32 s59, v254, 54
.LBB0_3255:
	s_branch .LBB0_3257
.LBB0_3257:
	v_max_f32_e32 v2, v115, v115
	v_max_f32_e32 v19, v114, v114
	v_max_f32_e32 v2, v19, v2
	v_max3_f32 v2, v2, v116, v117
	v_max3_f32 v2, v2, v118, v119
	v_max3_f32 v2, v2, v120, v121
	v_max3_f32 v2, v2, v122, v123
	v_max3_f32 v2, v2, v124, v125
	v_max3_f32 v2, v2, v126, v127
	v_max3_f32 v2, v2, v128, v129
	v_max3_f32 v2, v2, v98, v99
	v_max3_f32 v2, v2, v100, v101
	v_max3_f32 v2, v2, v102, v103
	v_max3_f32 v2, v2, v104, v105
	v_max3_f32 v2, v2, v106, v107
	v_max3_f32 v2, v2, v108, v109
	v_max3_f32 v2, v2, v110, v111
	v_max3_f32 v2, v2, v112, v113
	v_mov_b32_e32 v19, v2
	s_nop 1
	v_permlane32_swap_b32_e32 v2, v19
	v_max_f32_e32 v19, v19, v19
	v_max_f32_e32 v2, v2, v2
	v_max_f32_e32 v2, v2, v19
	v_max_f32_e32 v20, v215, v215
	v_sub_f32_e32 v19, v2, v215
	v_max_f32_e32 v2, v20, v2
	v_sub_f32_e32 v20, v215, v2
	v_mul_f32_e32 v20, 0x3e0293ee, v20
	v_mul_f32_e32 v19, 0x3db504f3, v19
	v_exp_f32_e32 v20, v20
	v_cmp_ge_f32_e32 vcc, s91, v19
	s_cmp_eq_u64 vcc, exec
	s_cselect_b64 s[10:11], -1, 0
	s_barrier
	s_waitcnt vmcnt(0)
	v_cndmask_b32_e64 v216, v20, 1.0, s[10:11]
	v_cmp_gt_f32_e32 vcc, 1.0, v216
	s_waitcnt vmcnt(3)
	ds_write_b128 v196, v[4:7]
	s_waitcnt vmcnt(2)
	ds_write_b128 v197, v[8:11]
	s_waitcnt vmcnt(1)
	ds_write_b128 v207, v[12:15] offset:32768
	s_waitcnt vmcnt(0)
	ds_write_b128 v207, v[178:181] offset:40960
	s_cbranch_vccz .LBB0_3261
	s_and_saveexec_b64 s[12:13], s[4:5]
	ds_write_b32 v211, v216 offset:128
	s_or_b64 exec, exec, s[12:13]
	s_waitcnt lgkmcnt(0)
	ds_read_b128 v[20:23], v210 offset:224
	ds_read_b128 v[24:27], v210 offset:192
	ds_read_b128 v[28:31], v210 offset:160
	ds_read_b128 v[130:133], v210 offset:128
	s_waitcnt lgkmcnt(3)
	v_pk_mul_f32 v[96:97], v[96:97], v[22:23]
	s_waitcnt lgkmcnt(2)
	v_pk_mul_f32 v[92:93], v[92:93], v[26:27]
	s_waitcnt lgkmcnt(1)
	v_pk_mul_f32 v[88:89], v[88:89], v[30:31]
	s_waitcnt lgkmcnt(0)
	v_pk_mul_f32 v[84:85], v[84:85], v[132:133]
	v_pk_mul_f32 v[94:95], v[94:95], v[20:21]
	v_pk_mul_f32 v[90:91], v[90:91], v[24:25]
	v_pk_mul_f32 v[86:87], v[86:87], v[28:29]
	v_pk_mul_f32 v[82:83], v[82:83], v[130:131]
	v_pk_mul_f32 v[80:81], v[80:81], v[22:23]
	v_pk_mul_f32 v[76:77], v[76:77], v[26:27]
	v_pk_mul_f32 v[72:73], v[72:73], v[30:31]
	v_pk_mul_f32 v[68:69], v[68:69], v[132:133]
	v_pk_mul_f32 v[78:79], v[78:79], v[20:21]
	v_pk_mul_f32 v[74:75], v[74:75], v[24:25]
	v_pk_mul_f32 v[70:71], v[70:71], v[28:29]
	v_pk_mul_f32 v[66:67], v[66:67], v[130:131]
	v_pk_mul_f32 v[64:65], v[64:65], v[22:23]
	v_pk_mul_f32 v[60:61], v[60:61], v[26:27]
	v_pk_mul_f32 v[56:57], v[56:57], v[30:31]
	v_pk_mul_f32 v[52:53], v[52:53], v[132:133]
	v_pk_mul_f32 v[62:63], v[62:63], v[20:21]
	v_pk_mul_f32 v[58:59], v[58:59], v[24:25]
	v_pk_mul_f32 v[54:55], v[54:55], v[28:29]
	v_pk_mul_f32 v[50:51], v[50:51], v[130:131]
	v_pk_mul_f32 v[48:49], v[48:49], v[22:23]
	v_pk_mul_f32 v[44:45], v[44:45], v[26:27]
	v_pk_mul_f32 v[40:41], v[40:41], v[30:31]
	v_pk_mul_f32 v[36:37], v[36:37], v[132:133]
	v_pk_mul_f32 v[46:47], v[46:47], v[20:21]
	v_pk_mul_f32 v[42:43], v[42:43], v[24:25]
	v_pk_mul_f32 v[38:39], v[38:39], v[28:29]
	v_pk_mul_f32 v[34:35], v[34:35], v[130:131]

.LBB0_3276:
	s_andn2_b64 vcc, exec, s[8:9]
	s_cbranch_vccnz .LBB0_3284
	s_mov_b64 s[8:9], -1
	s_and_b64 vcc, exec, s[10:11]
	s_cbranch_vccz .LBB0_3279
	v_bfe_u32 v2, v213, s16, 1
	v_cmp_eq_u32_e32 vcc, 0, v2
	s_mov_b64 s[8:9], 0
	s_nop 0
	v_cndmask_b32_e32 v114, v114, v18, vcc
	v_cndmask_b32_e32 v98, v98, v18, vcc
	v_cndmask_b32_e32 v115, v115, v18, vcc
	v_cndmask_b32_e32 v99, v99, v18, vcc
	v_cndmask_b32_e32 v116, v116, v18, vcc
	v_cndmask_b32_e32 v100, v100, v18, vcc
	v_cndmask_b32_e32 v117, v117, v18, vcc
	v_cndmask_b32_e32 v101, v101, v18, vcc
	v_cndmask_b32_e32 v118, v118, v18, vcc
	v_cndmask_b32_e32 v102, v102, v18, vcc
	v_cndmask_b32_e32 v119, v119, v18, vcc
	v_cndmask_b32_e32 v103, v103, v18, vcc
	v_cndmask_b32_e32 v120, v120, v18, vcc
	v_cndmask_b32_e32 v104, v104, v18, vcc
	v_cndmask_b32_e32 v121, v121, v18, vcc
	v_cndmask_b32_e32 v105, v105, v18, vcc
	v_cndmask_b32_e32 v122, v122, v18, vcc
	v_cndmask_b32_e32 v106, v106, v18, vcc
	v_cndmask_b32_e32 v123, v123, v18, vcc
	v_cndmask_b32_e32 v107, v107, v18, vcc
	v_cndmask_b32_e32 v124, v124, v18, vcc
	v_cndmask_b32_e32 v108, v108, v18, vcc
	v_cndmask_b32_e32 v125, v125, v18, vcc
	v_cndmask_b32_e32 v109, v109, v18, vcc
	v_cndmask_b32_e32 v126, v126, v18, vcc
	v_cndmask_b32_e32 v110, v110, v18, vcc
	v_cndmask_b32_e32 v127, v127, v18, vcc
	v_cndmask_b32_e32 v111, v111, v18, vcc
	v_cndmask_b32_e32 v128, v128, v18, vcc
	v_cndmask_b32_e32 v112, v112, v18, vcc
	v_cndmask_b32_e32 v129, v129, v18, vcc
	v_cndmask_b32_e32 v113, v113, v18, vcc
.LBB0_3279:
	s_andn2_b64 vcc, exec, s[8:9]
	s_cbranch_vccnz .LBB0_3284
	s_or_b32 s8, s3, 63
	s_cmp_le_i32 s8, s82
	s_cbranch_scc1 .LBB0_3282
	v_subrev_u32_e32 v2, s3, v214
	v_cmp_gt_i32_e64 s[66:67], 26, v2
	v_cmp_gt_i32_e64 s[68:69], 27, v2
	v_cmp_gt_i32_e64 s[64:65], 25, v2
	s_and_b64 s[66:67], s[68:69], s[66:67]
	v_cmp_gt_i32_e64 s[62:63], 24, v2
	s_and_b64 s[64:65], s[66:67], s[64:65]
	v_cmp_gt_i32_e64 s[60:61], 19, v2
	s_and_b64 s[62:63], s[64:65], s[62:63]
	v_cmp_gt_i32_e64 s[58:59], 18, v2
	s_and_b64 s[60:61], s[62:63], s[60:61]
	v_cmp_gt_i32_e64 s[56:57], 17, v2
	s_and_b64 s[58:59], s[60:61], s[58:59]
	v_cmp_gt_i32_e64 s[54:55], 16, v2
	s_and_b64 s[56:57], s[58:59], s[56:57]
	v_cmp_gt_i32_e64 s[52:53], 11, v2
	s_and_b64 s[54:55], s[56:57], s[54:55]
	v_cmp_gt_i32_e64 s[50:51], 10, v2
	s_and_b64 s[52:53], s[54:55], s[52:53]
	v_cmp_gt_i32_e64 s[48:49], 9, v2
	s_and_b64 s[50:51], s[52:53], s[50:51]
	v_cmp_gt_i32_e64 s[46:47], 8, v2
	s_and_b64 s[48:49], s[50:51], s[48:49]
	v_cmp_gt_i32_e64 s[44:45], 3, v2
	s_and_b64 s[46:47], s[48:49], s[46:47]
	v_cmp_gt_i32_e64 s[42:43], 2, v2
	s_and_b64 s[44:45], s[46:47], s[44:45]
	v_cmp_gt_i32_e64 s[40:41], 1, v2
	s_and_b64 s[42:43], s[44:45], s[42:43]
	v_cmp_gt_i32_e64 s[38:39], 0, v2
	s_and_b64 s[40:41], s[42:43], s[40:41]
	s_and_b64 s[38:39], s[40:41], s[38:39]
	v_cmp_gt_i32_e64 s[36:37], 58, v2
	v_cndmask_b32_e64 v114, v114, v18, s[38:39]
	v_cmp_gt_i32_e64 s[38:39], 59, v2
	v_cmp_gt_i32_e64 s[34:35], 57, v2
	s_and_b64 s[36:37], s[38:39], s[36:37]
	v_cmp_gt_i32_e64 s[30:31], 56, v2
	s_and_b64 s[34:35], s[36:37], s[34:35]
	v_cmp_gt_i32_e64 s[28:29], 51, v2
	s_and_b64 s[30:31], s[34:35], s[30:31]
	v_cmp_gt_i32_e64 s[26:27], 50, v2
	s_and_b64 s[28:29], s[30:31], s[28:29]
	v_cmp_gt_i32_e64 s[24:25], 49, v2
	s_and_b64 s[26:27], s[28:29], s[26:27]
	v_cmp_gt_i32_e64 s[22:23], 48, v2
	s_and_b64 s[24:25], s[26:27], s[24:25]
	v_cmp_gt_i32_e64 s[20:21], 43, v2
	s_and_b64 s[22:23], s[24:25], s[22:23]
	v_cmp_gt_i32_e64 s[18:19], 42, v2
	s_and_b64 s[20:21], s[22:23], s[20:21]
	v_cmp_gt_i32_e64 s[16:17], 41, v2
	s_and_b64 s[18:19], s[20:21], s[18:19]
	v_cmp_gt_i32_e64 s[14:15], 40, v2
	s_and_b64 s[16:17], s[18:19], s[16:17]
	v_cmp_gt_i32_e64 s[12:13], 35, v2
	s_and_b64 s[14:15], s[16:17], s[14:15]
	v_cmp_gt_i32_e64 s[10:11], 34, v2
	s_and_b64 s[12:13], s[14:15], s[12:13]
	v_cmp_gt_i32_e64 s[8:9], 33, v2
	s_and_b64 s[10:11], s[12:13], s[10:11]
	v_cmp_gt_i32_e32 vcc, 32, v2
	s_and_b64 s[8:9], s[10:11], s[8:9]
	v_cndmask_b32_e64 v128, v128, v18, s[66:67]
	v_cndmask_b32_e64 v127, v127, v18, s[64:65]
	v_cndmask_b32_e64 v126, v126, v18, s[62:63]
	v_cndmask_b32_e64 v125, v125, v18, s[60:61]
	v_readlane_b32 s60, v254, 55
	v_cndmask_b32_e64 v124, v124, v18, s[58:59]
	v_cndmask_b32_e64 v123, v123, v18, s[56:57]
	v_readlane_b32 s56, v254, 51
	s_and_b64 vcc, s[8:9], vcc
	v_cndmask_b32_e64 v129, v129, v18, s[68:69]
	v_readlane_b32 s61, v254, 56
	v_readlane_b32 s57, v254, 52
	v_cndmask_b32_e64 v122, v122, v18, s[54:55]
	v_cndmask_b32_e64 v121, v121, v18, s[52:53]
	v_cndmask_b32_e64 v120, v120, v18, s[50:51]
	v_cndmask_b32_e64 v119, v119, v18, s[48:49]
	v_cndmask_b32_e64 v118, v118, v18, s[46:47]
	v_cndmask_b32_e64 v117, v117, v18, s[44:45]
	v_cndmask_b32_e64 v116, v116, v18, s[42:43]
	v_cndmask_b32_e64 v115, v115, v18, s[40:41]
	v_cndmask_b32_e64 v113, v113, v18, s[38:39]
	v_cndmask_b32_e64 v112, v112, v18, s[36:37]
	v_cndmask_b32_e64 v111, v111, v18, s[34:35]
	v_cndmask_b32_e64 v110, v110, v18, s[30:31]
	v_cndmask_b32_e64 v109, v109, v18, s[28:29]
	v_cndmask_b32_e64 v108, v108, v18, s[26:27]
	v_cndmask_b32_e64 v107, v107, v18, s[24:25]
	v_cndmask_b32_e64 v106, v106, v18, s[22:23]
	v_cndmask_b32_e64 v105, v105, v18, s[20:21]
	v_cndmask_b32_e64 v104, v104, v18, s[18:19]
	v_cndmask_b32_e64 v103, v103, v18, s[16:17]
	v_cndmask_b32_e64 v102, v102, v18, s[14:15]
	v_cndmask_b32_e64 v101, v101, v18, s[12:13]
	v_cndmask_b32_e64 v100, v100, v18, s[10:11]
	v_cndmask_b32_e64 v99, v99, v18, s[8:9]
	v_cndmask_b32_e32 v98, v98, v18, vcc
	v_readlane_b32 s62, v254, 57
	v_readlane_b32 s63, v254, 58
	v_readlane_b32 s64, v254, 59
	v_readlane_b32 s65, v254, 60
	v_readlane_b32 s66, v254, 61
	v_readlane_b32 s67, v254, 62
	v_readlane_b32 s58, v254, 53
	v_readlane_b32 s59, v254, 54
.LBB0_3282:
	s_branch .LBB0_3284
.LBB0_3284:
	v_max_f32_e32 v2, v115, v115
	v_max_f32_e32 v20, v114, v114
	v_max_f32_e32 v2, v20, v2
	v_max3_f32 v2, v2, v116, v117
	v_max3_f32 v2, v2, v118, v119
	v_max3_f32 v2, v2, v120, v121
	v_max3_f32 v2, v2, v122, v123
	v_max3_f32 v2, v2, v124, v125
	v_max3_f32 v2, v2, v126, v127
	v_max3_f32 v2, v2, v128, v129
	v_max3_f32 v2, v2, v98, v99
	v_max3_f32 v2, v2, v100, v101
	v_max3_f32 v2, v2, v102, v103
	v_max3_f32 v2, v2, v104, v105
	v_max3_f32 v2, v2, v106, v107
	v_max3_f32 v2, v2, v108, v109
	v_max3_f32 v2, v2, v110, v111
	v_max3_f32 v2, v2, v112, v113
	v_mov_b32_e32 v20, v2
	s_nop 1
	v_permlane32_swap_b32_e32 v2, v20
	v_max_f32_e32 v20, v20, v20
	v_max_f32_e32 v2, v2, v2
	v_max_f32_e32 v2, v2, v20
	v_sub_f32_e32 v20, v2, v215
	v_mul_f32_e32 v20, 0x3db504f3, v20
	v_cmp_ge_f32_e32 vcc, s91, v20
	s_cmp_eq_u64 vcc, exec
	s_cselect_b64 s[8:9], -1, 0
	s_andn2_b64 vcc, exec, s[70:71]
	s_barrier
	s_cbranch_vccnz .LBB0_3286
	s_waitcnt vmcnt(0)
	s_waitcnt vmcnt(3)
	ds_write_b128 v196, v[4:7] offset:16384
	s_waitcnt vmcnt(2)
	ds_write_b128 v197, v[8:11] offset:16384
	s_waitcnt vmcnt(1)
	ds_write_b128 v207, v[12:15] offset:49152
	s_waitcnt vmcnt(0)
	ds_write_b128 v207, v[178:181] offset:57344
